# combined: gemm prologue reorder + barrier leader reorder + init x->bf16 loop 4x unrolled + kind-major k0 unit order
# baseline (speedup 1.0000x reference)
.LBB0_29:
	global_load_dwordx4 v[8:11], v[4:5], off offset:-16
	global_load_dwordx4 v[16:19], v[4:5], off
	v_lshl_add_u64 v[70:71], v[4:5], 0, s[12:13]
	global_load_dwordx4 v[20:23], v[70:71], off offset:-16
	global_load_dwordx4 v[24:27], v[70:71], off
	v_lshl_add_u64 v[72:73], v[70:71], 0, s[12:13]
	global_load_dwordx4 v[28:31], v[72:73], off offset:-16
	global_load_dwordx4 v[32:35], v[72:73], off
	v_lshl_add_u64 v[74:75], v[72:73], 0, s[12:13]
	global_load_dwordx4 v[76:79], v[74:75], off offset:-16
	global_load_dwordx4 v[80:83], v[74:75], off
	v_lshl_add_u64 v[4:5], v[74:75], 0, s[12:13]
	v_add_u32_e32 v2, s24, v2
	v_add_u32_e32 v2, s24, v2
	v_add_u32_e32 v2, s24, v2
	v_add_u32_e32 v2, s24, v2
	v_cmp_lt_i32_e32 vcc, s2, v2
	s_or_b64 s[16:17], vcc, s[16:17]
	s_waitcnt vmcnt(6)
	v_cvt_pk_bf16_f32 v8, v8, v9
	v_cvt_pk_bf16_f32 v9, v10, v11
	v_cvt_pk_bf16_f32 v10, v16, v17
	v_cvt_pk_bf16_f32 v11, v18, v19
	global_store_dwordx4 v[6:7], v[8:11], off
	v_lshl_add_u64 v[84:85], v[6:7], 0, s[14:15]
	s_waitcnt vmcnt(5)
	v_cvt_pk_bf16_f32 v20, v20, v21
	v_cvt_pk_bf16_f32 v21, v22, v23
	v_cvt_pk_bf16_f32 v22, v24, v25
	v_cvt_pk_bf16_f32 v23, v26, v27
	global_store_dwordx4 v[84:85], v[20:23], off
	v_lshl_add_u64 v[86:87], v[84:85], 0, s[14:15]
	s_waitcnt vmcnt(4)
	v_cvt_pk_bf16_f32 v28, v28, v29
	v_cvt_pk_bf16_f32 v29, v30, v31
	v_cvt_pk_bf16_f32 v30, v32, v33
	v_cvt_pk_bf16_f32 v31, v34, v35
	global_store_dwordx4 v[86:87], v[28:31], off
	v_lshl_add_u64 v[88:89], v[86:87], 0, s[14:15]
	s_waitcnt vmcnt(3)
	v_cvt_pk_bf16_f32 v76, v76, v77
	v_cvt_pk_bf16_f32 v77, v78, v79
	v_cvt_pk_bf16_f32 v78, v80, v81
	v_cvt_pk_bf16_f32 v79, v82, v83
	global_store_dwordx4 v[88:89], v[76:79], off
	v_lshl_add_u64 v[6:7], v[88:89], 0, s[14:15]
	s_andn2_b64 exec, exec, s[16:17]
	s_cbranch_execnz .LBB0_29

.LBB0_147:
	s_load_dwordx2 s[36:37], s[36:37], 0x10
	s_and_b64 vcc, exec, s[26:27]
	s_cbranch_vccz .LBB0_166
	s_and_b32 s5, s3, 7
	s_lshl_b32 s5, s5, 3
	s_bfe_u32 s7, s3, 0x30008
	s_lshl_b32 s7, s7, 2
	s_lshr_b32 s7, 0x1430652, s7
	s_and_b32 s7, s7, 15
	s_mov_b32 s8, s7
	s_mov_b32 s9, 0
	s_or_b32 s5, s5, s6
	s_cmp_gt_i32 s7, 1
	s_cselect_b64 s[6:7], -1, 0
	s_cmp_lg_u64 s[6:7], 0
	s_addc_u32 s6, s9, s8
	s_lshl_b32 s6, s6, 2
	s_bfe_u32 s7, s3, 0x20006
	s_or_b32 s6, s6, s7
	s_cmp_lt_i32 s6, 24
	s_cselect_b32 s7, 8, 12
	s_cmp_gt_i32 s6, 7
	s_cselect_b32 s7, s7, 0
	s_add_i32 s44, s7, s6
	s_lshl_b32 s6, s5, 19
	s_add_u32 s34, s70, s6
	s_addc_u32 s35, s71, 0
	s_ashr_i32 s45, s44, 31
	s_lshl_b64 s[6:7], s[44:45], 19
	s_add_u32 s38, s74, s6
	s_addc_u32 s39, s75, s7
	s_cmp_lt_i32 s44, 4
	s_mov_b32 s45, 0
	s_cbranch_scc1 .LBB0_165
	s_cmp_gt_u32 s44, 7
	s_mov_b64 s[26:27], -1
	s_cbranch_scc0 .LBB0_162
	s_cmp_gt_u32 s44, 23
	s_cbranch_scc0 .LBB0_159
	s_lshl_b32 s7, s44, 8
	s_cmp_gt_u32 s44, 27
	s_cbranch_scc0 .LBB0_156
	s_cmp_gt_u32 s44, 31
	s_cbranch_scc0 .LBB0_154
	s_add_i32 s6, s7, 0xffffdc00
	s_mov_b64 s[26:27], 0

.LBB0_179:
	s_and_b64 vcc, exec, s[26:27]
	s_cbranch_vccz .LBB0_199
	s_and_b32 s6, s3, 7
	s_lshl_b32 s6, s6, 3
	s_bfe_u32 s9, s3, 0x30008
	s_lshl_b32 s9, s9, 2
	s_lshr_b32 s9, 0x1430652, s9
	s_and_b32 s9, s9, 15
	s_mov_b32 s5, s9
	s_mov_b32 s10, 0
	s_or_b32 s40, s6, s8
	s_cmp_gt_i32 s9, 1
	s_cselect_b64 s[8:9], -1, 0
	s_cmp_lg_u64 s[8:9], 0
	s_addc_u32 s5, s10, s5
	s_lshl_b32 s5, s5, 2
	s_bfe_u32 s6, s3, 0x20006
	s_or_b32 s5, s5, s6
	s_cmp_lt_i32 s5, 24
	s_cselect_b32 s6, 8, 12
	s_cmp_gt_i32 s5, 7
	s_cselect_b32 s6, s6, 0
	s_ashr_i32 s41, s40, 31
	s_add_i32 s50, s6, s5
	s_lshl_b64 s[8:9], s[40:41], 19
	s_add_u32 s54, s70, s8
	s_addc_u32 s55, s71, s9
	s_ashr_i32 s51, s50, 31
	s_lshl_b64 s[8:9], s[50:51], 19
	s_add_u32 s56, s74, s8
	s_addc_u32 s57, s75, s9
	s_cmp_lt_i32 s50, 4
	s_mov_b32 s5, 0
	s_cbranch_scc1 .LBB0_197
	s_cmp_gt_u32 s50, 7
	s_mov_b64 s[26:27], -1
	s_cbranch_scc0 .LBB0_194
	s_cmp_gt_u32 s50, 23
	s_cbranch_scc0 .LBB0_191
	s_lshl_b32 s8, s50, 8
	s_cmp_gt_u32 s50, 27
	s_cbranch_scc0 .LBB0_188
	s_cmp_gt_u32 s50, 31
	s_cbranch_scc0 .LBB0_186
	s_add_i32 s6, s8, 0xffffdc00
	s_mov_b64 s[26:27], 0
